# baseline (speedup 1.0000x reference)
_Z8knn_gemmPKcS0_Pi:
	s_ashr_i32 s3, s2, 31
	s_lshr_b32 s3, s3, 29
	s_add_i32 s3, s2, s3
	s_ashr_i32 s4, s3, 3
	s_and_b32 s3, s3, -8
	s_sub_i32 s3, s2, s3
	s_cmp_lt_i32 s3, 0
	s_movk_i32 s12, 0x188
	s_cselect_b32 s5, s12, 0x187
	s_mul_i32 s3, s5, s3
	s_add_i32 s3, s3, s4
	s_ashr_i32 s4, s3, 31
	s_lshr_b32 s4, s4, 27
	s_add_i32 s10, s3, s4
	s_ashr_i32 s4, s10, 5
	s_lshl_b32 s11, s4, 2
	s_sub_i32 s4, 0x187, s11
	s_min_i32 s13, s4, 4
	s_abs_i32 s14, s13
	v_cvt_f32_u32_e32 v1, s14
	s_andn2_b32 s10, s10, 31
	s_load_dwordx4 s[4:7], s[0:1], 0x0
	s_load_dwordx2 s[8:9], s[0:1], 0x10
	s_sub_i32 s0, s3, s10
	v_rcp_iflag_f32_e32 v1, v1
	s_sub_i32 s10, 0, s14
	s_abs_i32 s3, s0
	s_xor_b32 s1, s0, s13
	v_mul_f32_e32 v1, 0x4f7ffffe, v1
	v_cvt_u32_f32_e32 v1, v1
	s_ashr_i32 s1, s1, 31
	v_lshrrev_b32_e32 v2, 8, v0
	v_lshlrev_b32_e32 v168, 4, v0
	v_readfirstlane_b32 s15, v1
	s_mul_i32 s10, s10, s15
	s_mul_hi_u32 s10, s15, s10
	s_add_i32 s15, s15, s10
	s_mul_hi_u32 s10, s3, s15
	s_mul_i32 s15, s10, s14
	s_sub_i32 s3, s3, s15
	s_add_i32 s15, s10, 1
	s_sub_i32 s16, s3, s14
	s_cmp_ge_u32 s3, s14
	s_cselect_b32 s10, s15, s10
	s_cselect_b32 s3, s16, s3
	s_add_i32 s15, s10, 1
	s_cmp_ge_u32 s3, s14
	s_cselect_b32 s3, s15, s10
	s_xor_b32 s3, s3, s1
	s_sub_i32 s34, s3, s1
	s_mul_i32 s1, s34, s13
	s_sub_i32 s0, s0, s1
	s_add_i32 s11, s11, s0
	v_readfirstlane_b32 s1, v0
	s_sub_i32 s13, 0x186, s11
	s_lshl_b32 s3, s1, 4
	s_mul_i32 s10, s34, 0x30000
	s_mul_hi_i32 s1, s34, 0x30000
	s_waitcnt lgkmcnt(0)
	s_add_u32 s10, s6, s10
	s_addc_u32 s11, s7, s1
	s_mul_i32 s14, s13, 0x30000
	s_mul_hi_i32 s1, s13, 0x30000
	s_add_u32 s22, s4, s14
	v_readfirstlane_b32 s0, v2
	s_addc_u32 s23, s5, s1
	s_cmp_eq_u32 s0, 0
	s_cselect_b64 s[0:1], -1, 0
	s_add_u32 s16, s10, 0x2000
	s_addc_u32 s17, s11, 0
	s_add_u32 s18, s22, 0xfffff000
	s_addc_u32 s19, s23, -1
	s_and_b64 s[14:15], s[0:1], exec
	s_cselect_b32 s17, s17, s19
	s_cselect_b32 s16, s16, s18
	s_add_u32 s18, s22, 0x1000
	s_addc_u32 s19, s23, 0
	s_add_i32 s14, s3, 0
	s_mov_b64 s[20:21], s[10:11]
	s_add_i32 s15, s14, 0x2000
	v_lshrrev_b32_e32 v5, 2, v0
	v_lshrrev_b32_e32 v1, 4, v0
	s_add_i32 s16, s14, 0x4000
	v_and_b32_e32 v5, 2, v5
	s_add_u32 s18, s10, 0x3000
	s_addc_u32 s19, s11, 0
	s_add_u32 s3, s10, 0x5000
	s_addc_u32 s17, s11, 0
	s_add_u32 s20, s22, 0x2000
	s_addc_u32 s21, s23, 0
	s_and_b64 s[10:11], s[0:1], exec
	s_cselect_b32 s11, s17, s21
	s_cselect_b32 s10, s3, s20
	s_add_u32 s20, s22, 0x4000
	s_addc_u32 s21, s23, 0
	s_add_i32 s17, s14, 0x6000
	v_add_lshl_u32 v1, v5, v1, 3
	s_add_i32 s18, s14, 0x8000
	s_add_i32 s19, s14, 0xa000
	v_and_b32_e32 v3, 15, v0
	v_and_b32_e32 v5, 24, v1
	v_lshrrev_b32_e32 v1, 1, v0
	s_movk_i32 s3, 0x60
	s_add_i32 s20, s14, 0xc000
	v_and_or_b32 v1, v1, s3, v3
	v_lshl_or_b32 v2, v2, 6, v3
	s_add_u32 s21, s4, 0x12000
	v_and_b32_e32 v4, 48, v0
	v_mad_u32_u24 v6, v1, s3, 0
	v_mad_u32_u24 v2, v2, s3, 0
	s_addc_u32 s22, s5, 0
	v_add_u32_e32 v1, v6, v4
	v_add_u32_e32 v170, v2, v4
	v_add_u32_e32 v172, v6, v5
	v_add_u32_e32 v173, v2, v5
	v_mov_b32_e32 v39, 0
	s_add_u32 s23, s6, 0x12000
	v_add_u32_e32 v171, 0x3000, v170
	v_add_u32_e32 v174, 0x3040, v173
	v_mov_b32_e32 v169, v39
	v_add_u32_e32 v175, 0x12000, v1
	v_add_u32_e32 v176, 0x12040, v172
	v_add_u32_e32 v177, 0x15000, v170
	v_add_u32_e32 v178, 0x15040, v173
	v_add_u32_e32 v179, 0x12600, v1
	v_add_u32_e32 v180, 0x12640, v172
	v_add_u32_e32 v181, 0x15600, v170
	v_add_u32_e32 v182, 0x15640, v173
	v_add_u32_e32 v183, 0x15c00, v170
	v_add_u32_e32 v184, 0x15c40, v173
	v_add_u32_e32 v185, 0x16200, v170
	v_add_u32_e32 v186, 0x16240, v173
	s_addc_u32 s24, s7, 0
	v_mov_b32_e32 v187, 0x7f7f7f7f
	s_add_i32 s25, 0, 0x18000
	s_movk_i32 s26, 0xff80
	s_movk_i32 s27, 0x30e
	s_add_i32 s28, s14, 0xe000
	s_add_i32 s29, s20, 0x4000
	s_add_i32 s30, s14, 0x12000
	s_add_i32 s31, s14, 0x14000
	s_add_i32 s33, s14, 0x16000
	s_lshr_b32 s66, s14, 12
	s_and_b32 s54, s14, 0xfff
	s_mul_i32 s67, s66, 0x6000
	s_add_i32 s54, s54, s67
	s_add_i32 s55, s54, 0x1000
	s_add_i32 s56, s54, 0x2000
	s_add_i32 s57, s54, 0x3000
	s_add_i32 s58, s54, 0x4000
	s_add_i32 s59, s54, 0x5000
	s_add_i32 s60, s54, 0xc000
	s_add_i32 s61, s54, 0xd000
	s_add_i32 s62, s54, 0xe000
	s_add_i32 s63, s54, 0xf000
	s_add_i32 s64, s54, 0x10000
	s_add_i32 s65, s54, 0x11000
	v_and_b32_e32 v228, 0xfff, v168
	v_add_u32_e32 v229, 0x1000, v228
	v_add_u32_e32 v230, 0x2000, v228
	s_mul_i32 s68, s34, 0x30000
	s_mul_hi_i32 s69, s34, 0x30000
	s_add_u32 s68, s6, s68
	s_addc_u32 s69, s7, s69
	s_mul_i32 s70, s13, 0x30000
	s_mul_hi_i32 s71, s13, 0x30000
	s_add_u32 s70, s4, s70
	s_addc_u32 s71, s5, s71
	s_mul_i32 s67, s66, 0x3000
	s_add_u32 s68, s68, s67
	s_addc_u32 s69, s69, 0
	s_add_u32 s70, s70, s67
	s_addc_u32 s71, s71, 0
	s_mov_b32 m0, s54
	s_nop 0
	global_load_lds_dwordx4 v228, s[68:69]
	s_mov_b32 m0, s55
	s_nop 0
	global_load_lds_dwordx4 v229, s[68:69]
	s_mov_b32 m0, s56
	s_nop 0
	global_load_lds_dwordx4 v230, s[68:69]
	s_mov_b32 m0, s57
	s_nop 0
	global_load_lds_dwordx4 v228, s[70:71]
	s_mov_b32 m0, s58
	s_nop 0
	global_load_lds_dwordx4 v229, s[70:71]
	s_mov_b32 m0, s59
	s_nop 0
	global_load_lds_dwordx4 v230, s[70:71]
	s_cmp_eq_u32 s66, 0
	s_cbranch_scc0 .Lprio_g1
	s_setprio 2
	s_branch .LBB1_2

.Lgemm_peel:
	ds_read_b128 v[188:191], v1 offset:24576
	ds_read_b64 v[192:193], v172 offset:24640
	ds_read_b128 v[194:197], v1 offset:26112
	ds_read_b64 v[198:199], v172 offset:26176
	ds_read_b128 v[200:203], v170 offset:36864
	ds_read_b64 v[204:205], v173 offset:36928
	ds_read_b128 v[206:209], v170 offset:38400
	ds_read_b64 v[210:211], v173 offset:38464
	ds_read_b128 v[212:215], v170 offset:39936
	ds_read_b64 v[216:217], v173 offset:40000
	ds_read_b128 v[218:221], v170 offset:41472
	ds_read_b64 v[222:223], v173 offset:41536
	v_mfma_scale_f32_16x16x128_f8f6f4 v[164:167], v[2:7], v[20:25], 0, v187, v187 op_sel_hi:[0,0,0] cbsz:2 blgp:2
	v_mfma_scale_f32_16x16x128_f8f6f4 v[160:163], v[8:13], v[20:25], 0, v187, v187 op_sel_hi:[0,0,0] cbsz:2 blgp:2
	v_mfma_scale_f32_16x16x128_f8f6f4 v[156:159], v[14:19], v[20:25], 0, v187, v187 op_sel_hi:[0,0,0] cbsz:2 blgp:2
	v_mfma_scale_f32_16x16x128_f8f6f4 v[152:155], v[26:31], v[20:25], 0, v187, v187 op_sel_hi:[0,0,0] cbsz:2 blgp:2
	v_mfma_scale_f32_16x16x128_f8f6f4 v[148:151], v[2:7], v[32:37], 0, v187, v187 op_sel_hi:[0,0,0] cbsz:2 blgp:2
	v_mfma_scale_f32_16x16x128_f8f6f4 v[140:143], v[8:13], v[32:37], 0, v187, v187 op_sel_hi:[0,0,0] cbsz:2 blgp:2
	v_mfma_scale_f32_16x16x128_f8f6f4 v[132:135], v[14:19], v[32:37], 0, v187, v187 op_sel_hi:[0,0,0] cbsz:2 blgp:2
	v_mfma_scale_f32_16x16x128_f8f6f4 v[124:127], v[26:31], v[32:37], 0, v187, v187 op_sel_hi:[0,0,0] cbsz:2 blgp:2
	s_cmp_eq_u32 s66, 0
	s_cbranch_scc0 .Lpst0_other
	s_add_u32 s38, s2, 0xffffa000
	s_addc_u32 s39, s3, -1
	s_add_u32 s40, s11, 0xffffa000
	s_addc_u32 s41, s35, -1
	s_waitcnt vmcnt(0)
	s_barrier
	s_mov_b32 m0, s54
	s_nop 0
	global_load_lds_dwordx4 v228, s[38:39]
	s_mov_b32 m0, s55
	s_nop 0
	global_load_lds_dwordx4 v229, s[38:39]
	s_mov_b32 m0, s56
	s_nop 0
	global_load_lds_dwordx4 v230, s[38:39]
	s_mov_b32 m0, s57
	s_nop 0
	global_load_lds_dwordx4 v228, s[40:41]
	s_mov_b32 m0, s58
	s_nop 0
	global_load_lds_dwordx4 v229, s[40:41]
	s_mov_b32 m0, s59
	s_nop 0
	global_load_lds_dwordx4 v230, s[40:41]
	s_branch .Lpst0_join

.Lpst0_join:
	s_waitcnt lgkmcnt(0)
	v_mfma_scale_f32_16x16x128_f8f6f4 v[112:115], v[2:7], v[188:193], 0, v187, v187 op_sel_hi:[0,0,0] cbsz:2 blgp:2
	v_mfma_scale_f32_16x16x128_f8f6f4 v[100:103], v[8:13], v[188:193], 0, v187, v187 op_sel_hi:[0,0,0] cbsz:2 blgp:2
	v_mfma_scale_f32_16x16x128_f8f6f4 v[92:95], v[14:19], v[188:193], 0, v187, v187 op_sel_hi:[0,0,0] cbsz:2 blgp:2
	v_mfma_scale_f32_16x16x128_f8f6f4 v[88:91], v[26:31], v[188:193], 0, v187, v187 op_sel_hi:[0,0,0] cbsz:2 blgp:2
	v_mfma_scale_f32_16x16x128_f8f6f4 v[84:87], v[2:7], v[194:199], 0, v187, v187 op_sel_hi:[0,0,0] cbsz:2 blgp:2
	v_mfma_scale_f32_16x16x128_f8f6f4 v[76:79], v[8:13], v[194:199], 0, v187, v187 op_sel_hi:[0,0,0] cbsz:2 blgp:2
	v_mfma_scale_f32_16x16x128_f8f6f4 v[68:71], v[14:19], v[194:199], 0, v187, v187 op_sel_hi:[0,0,0] cbsz:2 blgp:2
	v_mfma_scale_f32_16x16x128_f8f6f4 v[60:63], v[26:31], v[194:199], 0, v187, v187 op_sel_hi:[0,0,0] cbsz:2 blgp:2
	ds_read_b128 v[2:5], v170 offset:61440
	ds_read_b64 v[6:7], v173 offset:61504
	ds_read_b128 v[8:11], v170 offset:62976
	ds_read_b64 v[12:13], v173 offset:63040
	ds_read_b128 v[14:17], v170 offset:64512
	ds_read_b64 v[18:19], v173 offset:64576
	ds_read_b128 v[26:29], v171 offset:53760
	ds_read_b64 v[30:31], v174 offset:53760
	v_mfma_scale_f32_16x16x128_f8f6f4 v[144:147], v[200:205], v[20:25], 0, v187, v187 op_sel_hi:[0,0,0] cbsz:2 blgp:2
	v_mfma_scale_f32_16x16x128_f8f6f4 v[136:139], v[206:211], v[20:25], 0, v187, v187 op_sel_hi:[0,0,0] cbsz:2 blgp:2
	v_mfma_scale_f32_16x16x128_f8f6f4 v[128:131], v[212:217], v[20:25], 0, v187, v187 op_sel_hi:[0,0,0] cbsz:2 blgp:2
	v_mfma_scale_f32_16x16x128_f8f6f4 v[120:123], v[218:223], v[20:25], 0, v187, v187 op_sel_hi:[0,0,0] cbsz:2 blgp:2
	v_mfma_scale_f32_16x16x128_f8f6f4 v[116:119], v[200:205], v[32:37], 0, v187, v187 op_sel_hi:[0,0,0] cbsz:2 blgp:2
	v_mfma_scale_f32_16x16x128_f8f6f4 v[108:111], v[206:211], v[32:37], 0, v187, v187 op_sel_hi:[0,0,0] cbsz:2 blgp:2
	v_mfma_scale_f32_16x16x128_f8f6f4 v[104:107], v[212:217], v[32:37], 0, v187, v187 op_sel_hi:[0,0,0] cbsz:2 blgp:2
	v_mfma_scale_f32_16x16x128_f8f6f4 v[96:99], v[218:223], v[32:37], 0, v187, v187 op_sel_hi:[0,0,0] cbsz:2 blgp:2
	ds_read_b128 v[20:23], v1 offset:49152
	ds_read_b64 v[24:25], v172 offset:49216
	ds_read_b128 v[32:35], v1 offset:50688
	ds_read_b64 v[36:37], v172 offset:50752
	s_cmp_eq_u32 s66, 1
	s_cbranch_scc0 .Lpst1_other
	s_add_u32 s38, s2, 0xffffd000
	s_addc_u32 s39, s3, -1
	s_add_u32 s40, s11, 0xffffd000
	s_addc_u32 s41, s35, -1
	s_waitcnt vmcnt(0)
	s_barrier
	s_mov_b32 m0, s54
	s_nop 0
	global_load_lds_dwordx4 v228, s[38:39]
	s_mov_b32 m0, s55
	s_nop 0
	global_load_lds_dwordx4 v229, s[38:39]
	s_mov_b32 m0, s56
	s_nop 0
	global_load_lds_dwordx4 v230, s[38:39]
	s_mov_b32 m0, s57
	s_nop 0
	global_load_lds_dwordx4 v228, s[40:41]
	s_mov_b32 m0, s58
	s_nop 0
	global_load_lds_dwordx4 v229, s[40:41]
	s_mov_b32 m0, s59
	s_nop 0
	global_load_lds_dwordx4 v230, s[40:41]
	s_branch .Lpst1_join

.Lpst1_join:
	v_mfma_scale_f32_16x16x128_f8f6f4 v[80:83], v[200:205], v[188:193], 0, v187, v187 op_sel_hi:[0,0,0] cbsz:2 blgp:2
	v_mfma_scale_f32_16x16x128_f8f6f4 v[72:75], v[206:211], v[188:193], 0, v187, v187 op_sel_hi:[0,0,0] cbsz:2 blgp:2
	v_mfma_scale_f32_16x16x128_f8f6f4 v[64:67], v[212:217], v[188:193], 0, v187, v187 op_sel_hi:[0,0,0] cbsz:2 blgp:2
	v_mfma_scale_f32_16x16x128_f8f6f4 v[56:59], v[218:223], v[188:193], 0, v187, v187 op_sel_hi:[0,0,0] cbsz:2 blgp:2
	v_mfma_scale_f32_16x16x128_f8f6f4 v[52:55], v[200:205], v[194:199], 0, v187, v187 op_sel_hi:[0,0,0] cbsz:2 blgp:2
	v_mfma_scale_f32_16x16x128_f8f6f4 v[224:227], v[206:211], v[194:199], 0, v187, v187 op_sel_hi:[0,0,0] cbsz:2 blgp:2
	v_mfma_scale_f32_16x16x128_f8f6f4 v[212:215], v[212:217], v[194:199], 0, v187, v187 op_sel_hi:[0,0,0] cbsz:2 blgp:2
	v_mfma_scale_f32_16x16x128_f8f6f4 v[216:219], v[218:223], v[194:199], 0, v187, v187 op_sel_hi:[0,0,0] cbsz:2 blgp:2
	s_waitcnt lgkmcnt(0)
	s_nop 0
	ds_read_b128 v[40:43], v175
	ds_read_b64 v[44:45], v176
	ds_read_b128 v[188:191], v179
	ds_read_b64 v[192:193], v180
	ds_read_b128 v[46:49], v177
	ds_read_b64 v[50:51], v178
	ds_read_b128 v[194:197], v181
	ds_read_b64 v[198:199], v182
	ds_read_b128 v[200:203], v183
	ds_read_b64 v[204:205], v184
	ds_read_b128 v[206:209], v185
	ds_read_b64 v[210:211], v186
	v_mfma_scale_f32_16x16x128_f8f6f4 v[164:167], v[2:7], v[20:25], v[164:167], v187, v187 op_sel_hi:[0,0,0] cbsz:2 blgp:2
	v_mfma_scale_f32_16x16x128_f8f6f4 v[160:163], v[8:13], v[20:25], v[160:163], v187, v187 op_sel_hi:[0,0,0] cbsz:2 blgp:2
	v_mfma_scale_f32_16x16x128_f8f6f4 v[156:159], v[14:19], v[20:25], v[156:159], v187, v187 op_sel_hi:[0,0,0] cbsz:2 blgp:2
	v_mfma_scale_f32_16x16x128_f8f6f4 v[152:155], v[26:31], v[20:25], v[152:155], v187, v187 op_sel_hi:[0,0,0] cbsz:2 blgp:2
	v_mfma_scale_f32_16x16x128_f8f6f4 v[148:151], v[2:7], v[32:37], v[148:151], v187, v187 op_sel_hi:[0,0,0] cbsz:2 blgp:2
	v_mfma_scale_f32_16x16x128_f8f6f4 v[140:143], v[8:13], v[32:37], v[140:143], v187, v187 op_sel_hi:[0,0,0] cbsz:2 blgp:2
	v_mfma_scale_f32_16x16x128_f8f6f4 v[132:135], v[14:19], v[32:37], v[132:135], v187, v187 op_sel_hi:[0,0,0] cbsz:2 blgp:2
	v_mfma_scale_f32_16x16x128_f8f6f4 v[124:127], v[26:31], v[32:37], v[124:127], v187, v187 op_sel_hi:[0,0,0] cbsz:2 blgp:2
	s_cmp_eq_u32 s66, 0
	s_cbranch_scc0 .Lpst2_other
	s_mov_b64 s[38:39], s[2:3]
	s_mov_b32 s40, s11
	s_mov_b32 s41, s35
	s_waitcnt vmcnt(0)
	s_barrier
	s_mov_b32 m0, s60
	s_nop 0
	global_load_lds_dwordx4 v228, s[38:39]
	s_mov_b32 m0, s61
	s_nop 0
	global_load_lds_dwordx4 v229, s[38:39]
	s_mov_b32 m0, s62
	s_nop 0
	global_load_lds_dwordx4 v230, s[38:39]
	s_mov_b32 m0, s63
	s_nop 0
	global_load_lds_dwordx4 v228, s[40:41]
	s_mov_b32 m0, s64
	s_nop 0
	global_load_lds_dwordx4 v229, s[40:41]
	s_mov_b32 m0, s65
	s_nop 0
	global_load_lds_dwordx4 v230, s[40:41]
	s_branch .Lpst2_join

.Lpst2_join:
	s_waitcnt lgkmcnt(0)
	v_mfma_scale_f32_16x16x128_f8f6f4 v[112:115], v[2:7], v[40:45], v[112:115], v187, v187 op_sel_hi:[0,0,0] cbsz:2 blgp:2
	v_mfma_scale_f32_16x16x128_f8f6f4 v[100:103], v[8:13], v[40:45], v[100:103], v187, v187 op_sel_hi:[0,0,0] cbsz:2 blgp:2
	v_mfma_scale_f32_16x16x128_f8f6f4 v[92:95], v[14:19], v[40:45], v[92:95], v187, v187 op_sel_hi:[0,0,0] cbsz:2 blgp:2
	v_mfma_scale_f32_16x16x128_f8f6f4 v[88:91], v[26:31], v[40:45], v[88:91], v187, v187 op_sel_hi:[0,0,0] cbsz:2 blgp:2
	v_mfma_scale_f32_16x16x128_f8f6f4 v[84:87], v[2:7], v[188:193], v[84:87], v187, v187 op_sel_hi:[0,0,0] cbsz:2 blgp:2
	v_mfma_scale_f32_16x16x128_f8f6f4 v[76:79], v[8:13], v[188:193], v[76:79], v187, v187 op_sel_hi:[0,0,0] cbsz:2 blgp:2
	v_mfma_scale_f32_16x16x128_f8f6f4 v[68:71], v[14:19], v[188:193], v[68:71], v187, v187 op_sel_hi:[0,0,0] cbsz:2 blgp:2
	v_mfma_scale_f32_16x16x128_f8f6f4 v[60:63], v[26:31], v[188:193], v[60:63], v187, v187 op_sel_hi:[0,0,0] cbsz:2 blgp:2
	ds_read_b128 v[2:5], v170 offset:12288
	ds_read_b64 v[6:7], v173 offset:12352
	ds_read_b128 v[8:11], v170 offset:13824
	ds_read_b64 v[12:13], v173 offset:13888
	ds_read_b128 v[14:17], v170 offset:15360
	ds_read_b64 v[18:19], v173 offset:15424
	ds_read_b128 v[26:29], v170 offset:16896
	ds_read_b64 v[30:31], v173 offset:16960
	v_mfma_scale_f32_16x16x128_f8f6f4 v[144:147], v[46:51], v[20:25], v[144:147], v187, v187 op_sel_hi:[0,0,0] cbsz:2 blgp:2
	v_mfma_scale_f32_16x16x128_f8f6f4 v[136:139], v[194:199], v[20:25], v[136:139], v187, v187 op_sel_hi:[0,0,0] cbsz:2 blgp:2
	v_mfma_scale_f32_16x16x128_f8f6f4 v[128:131], v[200:205], v[20:25], v[128:131], v187, v187 op_sel_hi:[0,0,0] cbsz:2 blgp:2
	v_mfma_scale_f32_16x16x128_f8f6f4 v[120:123], v[206:211], v[20:25], v[120:123], v187, v187 op_sel_hi:[0,0,0] cbsz:2 blgp:2
	v_mfma_scale_f32_16x16x128_f8f6f4 v[116:119], v[46:51], v[32:37], v[116:119], v187, v187 op_sel_hi:[0,0,0] cbsz:2 blgp:2
	v_mfma_scale_f32_16x16x128_f8f6f4 v[108:111], v[194:199], v[32:37], v[108:111], v187, v187 op_sel_hi:[0,0,0] cbsz:2 blgp:2
	v_mfma_scale_f32_16x16x128_f8f6f4 v[104:107], v[200:205], v[32:37], v[104:107], v187, v187 op_sel_hi:[0,0,0] cbsz:2 blgp:2
	v_mfma_scale_f32_16x16x128_f8f6f4 v[96:99], v[206:211], v[32:37], v[96:99], v187, v187 op_sel_hi:[0,0,0] cbsz:2 blgp:2
	ds_read_b128 v[20:23], v1
	ds_read_b64 v[24:25], v172 offset:64
	ds_read_b128 v[32:35], v1 offset:1536
	ds_read_b64 v[36:37], v172 offset:1600
	s_cmp_eq_u32 s66, 1
	s_cbranch_scc0 .Lpst3_other
	s_add_u32 s38, s2, 0x3000
	s_addc_u32 s39, s3, 0
	s_add_u32 s40, s11, 0x3000
	s_addc_u32 s41, s35, 0
	s_waitcnt vmcnt(0)
	s_barrier
	s_mov_b32 m0, s60
	s_nop 0
	global_load_lds_dwordx4 v228, s[38:39]
	s_mov_b32 m0, s61
	s_nop 0
	global_load_lds_dwordx4 v229, s[38:39]
	s_mov_b32 m0, s62
	s_nop 0
	global_load_lds_dwordx4 v230, s[38:39]
	s_mov_b32 m0, s63
	s_nop 0
	global_load_lds_dwordx4 v228, s[40:41]
	s_mov_b32 m0, s64
	s_nop 0
	global_load_lds_dwordx4 v229, s[40:41]
	s_mov_b32 m0, s65
	s_nop 0
	global_load_lds_dwordx4 v230, s[40:41]
	s_branch .Lpst3_join

.Lpst3_join:
	v_mfma_scale_f32_16x16x128_f8f6f4 v[80:83], v[46:51], v[40:45], v[80:83], v187, v187 op_sel_hi:[0,0,0] cbsz:2 blgp:2
	v_mfma_scale_f32_16x16x128_f8f6f4 v[72:75], v[194:199], v[40:45], v[72:75], v187, v187 op_sel_hi:[0,0,0] cbsz:2 blgp:2
	v_mfma_scale_f32_16x16x128_f8f6f4 v[64:67], v[200:205], v[40:45], v[64:67], v187, v187 op_sel_hi:[0,0,0] cbsz:2 blgp:2
	v_mfma_scale_f32_16x16x128_f8f6f4 v[56:59], v[206:211], v[40:45], v[56:59], v187, v187 op_sel_hi:[0,0,0] cbsz:2 blgp:2
	v_mfma_scale_f32_16x16x128_f8f6f4 v[52:55], v[46:51], v[188:193], v[52:55], v187, v187 op_sel_hi:[0,0,0] cbsz:2 blgp:2
	v_mfma_scale_f32_16x16x128_f8f6f4 v[48:51], v[194:199], v[188:193], v[224:227], v187, v187 op_sel_hi:[0,0,0] cbsz:2 blgp:2
	v_mfma_scale_f32_16x16x128_f8f6f4 v[44:47], v[200:205], v[188:193], v[212:215], v187, v187 op_sel_hi:[0,0,0] cbsz:2 blgp:2
	v_mfma_scale_f32_16x16x128_f8f6f4 v[40:43], v[206:211], v[188:193], v[216:219], v187, v187 op_sel_hi:[0,0,0] cbsz:2 blgp:2
	s_add_i32 s36, s36, 2
	s_add_u32 s11, s11, 0xc000
	s_addc_u32 s35, s35, 0
	s_add_u32 s2, s2, 0xc000
	s_addc_u32 s3, s3, 0
	s_cmp_lt_u32 s36, 4
	s_waitcnt lgkmcnt(0)
.LBB1_3:
	ds_read_b128 v[188:191], v1 offset:24576
	ds_read_b64 v[192:193], v172 offset:24640
	ds_read_b128 v[194:197], v1 offset:26112
	ds_read_b64 v[198:199], v172 offset:26176
	ds_read_b128 v[200:203], v170 offset:36864
	ds_read_b64 v[204:205], v173 offset:36928
	ds_read_b128 v[206:209], v170 offset:38400
	ds_read_b64 v[210:211], v173 offset:38464
	ds_read_b128 v[212:215], v170 offset:39936
	ds_read_b64 v[216:217], v173 offset:40000
	ds_read_b128 v[218:221], v170 offset:41472
	ds_read_b64 v[222:223], v173 offset:41536
	v_mfma_scale_f32_16x16x128_f8f6f4 v[164:167], v[2:7], v[20:25], v[164:167], v187, v187 op_sel_hi:[0,0,0] cbsz:2 blgp:2
	v_mfma_scale_f32_16x16x128_f8f6f4 v[160:163], v[8:13], v[20:25], v[160:163], v187, v187 op_sel_hi:[0,0,0] cbsz:2 blgp:2
	v_mfma_scale_f32_16x16x128_f8f6f4 v[156:159], v[14:19], v[20:25], v[156:159], v187, v187 op_sel_hi:[0,0,0] cbsz:2 blgp:2
	v_mfma_scale_f32_16x16x128_f8f6f4 v[152:155], v[26:31], v[20:25], v[152:155], v187, v187 op_sel_hi:[0,0,0] cbsz:2 blgp:2
	v_mfma_scale_f32_16x16x128_f8f6f4 v[148:151], v[2:7], v[32:37], v[148:151], v187, v187 op_sel_hi:[0,0,0] cbsz:2 blgp:2
	v_mfma_scale_f32_16x16x128_f8f6f4 v[140:143], v[8:13], v[32:37], v[140:143], v187, v187 op_sel_hi:[0,0,0] cbsz:2 blgp:2
	v_mfma_scale_f32_16x16x128_f8f6f4 v[132:135], v[14:19], v[32:37], v[132:135], v187, v187 op_sel_hi:[0,0,0] cbsz:2 blgp:2
	v_mfma_scale_f32_16x16x128_f8f6f4 v[124:127], v[26:31], v[32:37], v[124:127], v187, v187 op_sel_hi:[0,0,0] cbsz:2 blgp:2
	s_cmp_eq_u32 s66, 0
	s_cbranch_scc0 .Lst0_other
	s_add_u32 s38, s2, 0xffffa000
	s_addc_u32 s39, s3, -1
	s_add_u32 s40, s11, 0xffffa000
	s_addc_u32 s41, s35, -1
	s_waitcnt vmcnt(0)
	s_barrier
	s_mov_b32 m0, s54
	s_nop 0
	global_load_lds_dwordx4 v228, s[38:39]
	s_mov_b32 m0, s55
	s_nop 0
	global_load_lds_dwordx4 v229, s[38:39]
	s_mov_b32 m0, s56
	s_nop 0
	global_load_lds_dwordx4 v230, s[38:39]
	s_mov_b32 m0, s57
	s_nop 0
	global_load_lds_dwordx4 v228, s[40:41]
	s_mov_b32 m0, s58
	s_nop 0
	global_load_lds_dwordx4 v229, s[40:41]
	s_mov_b32 m0, s59
	s_nop 0
	global_load_lds_dwordx4 v230, s[40:41]
	s_branch .Lst0_join

.Lst0_join:
	s_waitcnt lgkmcnt(0)
	v_mfma_scale_f32_16x16x128_f8f6f4 v[112:115], v[2:7], v[188:193], v[112:115], v187, v187 op_sel_hi:[0,0,0] cbsz:2 blgp:2
	v_mfma_scale_f32_16x16x128_f8f6f4 v[100:103], v[8:13], v[188:193], v[100:103], v187, v187 op_sel_hi:[0,0,0] cbsz:2 blgp:2
	v_mfma_scale_f32_16x16x128_f8f6f4 v[92:95], v[14:19], v[188:193], v[92:95], v187, v187 op_sel_hi:[0,0,0] cbsz:2 blgp:2
	v_mfma_scale_f32_16x16x128_f8f6f4 v[88:91], v[26:31], v[188:193], v[88:91], v187, v187 op_sel_hi:[0,0,0] cbsz:2 blgp:2
	v_mfma_scale_f32_16x16x128_f8f6f4 v[84:87], v[2:7], v[194:199], v[84:87], v187, v187 op_sel_hi:[0,0,0] cbsz:2 blgp:2
	v_mfma_scale_f32_16x16x128_f8f6f4 v[76:79], v[8:13], v[194:199], v[76:79], v187, v187 op_sel_hi:[0,0,0] cbsz:2 blgp:2
	v_mfma_scale_f32_16x16x128_f8f6f4 v[68:71], v[14:19], v[194:199], v[68:71], v187, v187 op_sel_hi:[0,0,0] cbsz:2 blgp:2
	v_mfma_scale_f32_16x16x128_f8f6f4 v[60:63], v[26:31], v[194:199], v[60:63], v187, v187 op_sel_hi:[0,0,0] cbsz:2 blgp:2
	ds_read_b128 v[2:5], v170 offset:61440
	ds_read_b64 v[6:7], v173 offset:61504
	ds_read_b128 v[8:11], v170 offset:62976
	ds_read_b64 v[12:13], v173 offset:63040
	ds_read_b128 v[14:17], v170 offset:64512
	ds_read_b64 v[18:19], v173 offset:64576
	ds_read_b128 v[26:29], v171 offset:53760
	ds_read_b64 v[30:31], v174 offset:53760
	v_mfma_scale_f32_16x16x128_f8f6f4 v[144:147], v[200:205], v[20:25], v[144:147], v187, v187 op_sel_hi:[0,0,0] cbsz:2 blgp:2
	v_mfma_scale_f32_16x16x128_f8f6f4 v[136:139], v[206:211], v[20:25], v[136:139], v187, v187 op_sel_hi:[0,0,0] cbsz:2 blgp:2
	v_mfma_scale_f32_16x16x128_f8f6f4 v[128:131], v[212:217], v[20:25], v[128:131], v187, v187 op_sel_hi:[0,0,0] cbsz:2 blgp:2
	v_mfma_scale_f32_16x16x128_f8f6f4 v[120:123], v[218:223], v[20:25], v[120:123], v187, v187 op_sel_hi:[0,0,0] cbsz:2 blgp:2
	v_mfma_scale_f32_16x16x128_f8f6f4 v[116:119], v[200:205], v[32:37], v[116:119], v187, v187 op_sel_hi:[0,0,0] cbsz:2 blgp:2
	v_mfma_scale_f32_16x16x128_f8f6f4 v[108:111], v[206:211], v[32:37], v[108:111], v187, v187 op_sel_hi:[0,0,0] cbsz:2 blgp:2
	v_mfma_scale_f32_16x16x128_f8f6f4 v[104:107], v[212:217], v[32:37], v[104:107], v187, v187 op_sel_hi:[0,0,0] cbsz:2 blgp:2
	v_mfma_scale_f32_16x16x128_f8f6f4 v[96:99], v[218:223], v[32:37], v[96:99], v187, v187 op_sel_hi:[0,0,0] cbsz:2 blgp:2
	ds_read_b128 v[20:23], v1 offset:49152
	ds_read_b64 v[24:25], v172 offset:49216
	ds_read_b128 v[32:35], v1 offset:50688
	ds_read_b64 v[36:37], v172 offset:50752
	s_cmp_eq_u32 s66, 1
	s_cbranch_scc0 .Lst1_other
	s_add_u32 s38, s2, 0xffffd000
	s_addc_u32 s39, s3, -1
	s_add_u32 s40, s11, 0xffffd000
	s_addc_u32 s41, s35, -1
	s_waitcnt vmcnt(0)
	s_barrier
	s_mov_b32 m0, s54
	s_nop 0
	global_load_lds_dwordx4 v228, s[38:39]
	s_mov_b32 m0, s55
	s_nop 0
	global_load_lds_dwordx4 v229, s[38:39]
	s_mov_b32 m0, s56
	s_nop 0
	global_load_lds_dwordx4 v230, s[38:39]
	s_mov_b32 m0, s57
	s_nop 0
	global_load_lds_dwordx4 v228, s[40:41]
	s_mov_b32 m0, s58
	s_nop 0
	global_load_lds_dwordx4 v229, s[40:41]
	s_mov_b32 m0, s59
	s_nop 0
	global_load_lds_dwordx4 v230, s[40:41]
	s_branch .Lst1_join

.Lst1_join:
	v_mfma_scale_f32_16x16x128_f8f6f4 v[80:83], v[200:205], v[188:193], v[80:83], v187, v187 op_sel_hi:[0,0,0] cbsz:2 blgp:2
	v_mfma_scale_f32_16x16x128_f8f6f4 v[72:75], v[206:211], v[188:193], v[72:75], v187, v187 op_sel_hi:[0,0,0] cbsz:2 blgp:2
	v_mfma_scale_f32_16x16x128_f8f6f4 v[64:67], v[212:217], v[188:193], v[64:67], v187, v187 op_sel_hi:[0,0,0] cbsz:2 blgp:2
	v_mfma_scale_f32_16x16x128_f8f6f4 v[56:59], v[218:223], v[188:193], v[56:59], v187, v187 op_sel_hi:[0,0,0] cbsz:2 blgp:2
	v_mfma_scale_f32_16x16x128_f8f6f4 v[52:55], v[200:205], v[194:199], v[52:55], v187, v187 op_sel_hi:[0,0,0] cbsz:2 blgp:2
	v_mfma_scale_f32_16x16x128_f8f6f4 v[224:227], v[206:211], v[194:199], v[48:51], v187, v187 op_sel_hi:[0,0,0] cbsz:2 blgp:2
	v_mfma_scale_f32_16x16x128_f8f6f4 v[212:215], v[212:217], v[194:199], v[44:47], v187, v187 op_sel_hi:[0,0,0] cbsz:2 blgp:2
	v_mfma_scale_f32_16x16x128_f8f6f4 v[216:219], v[218:223], v[194:199], v[40:43], v187, v187 op_sel_hi:[0,0,0] cbsz:2 blgp:2
	s_waitcnt lgkmcnt(0)
	s_nop 0
	ds_read_b128 v[40:43], v175
	ds_read_b64 v[44:45], v176
	ds_read_b128 v[188:191], v179
	ds_read_b64 v[192:193], v180
	ds_read_b128 v[46:49], v177
	ds_read_b64 v[50:51], v178
	ds_read_b128 v[194:197], v181
	ds_read_b64 v[198:199], v182
	ds_read_b128 v[200:203], v183
	ds_read_b64 v[204:205], v184
	ds_read_b128 v[206:209], v185
	ds_read_b64 v[210:211], v186
	v_mfma_scale_f32_16x16x128_f8f6f4 v[164:167], v[2:7], v[20:25], v[164:167], v187, v187 op_sel_hi:[0,0,0] cbsz:2 blgp:2
	v_mfma_scale_f32_16x16x128_f8f6f4 v[160:163], v[8:13], v[20:25], v[160:163], v187, v187 op_sel_hi:[0,0,0] cbsz:2 blgp:2
	v_mfma_scale_f32_16x16x128_f8f6f4 v[156:159], v[14:19], v[20:25], v[156:159], v187, v187 op_sel_hi:[0,0,0] cbsz:2 blgp:2
	v_mfma_scale_f32_16x16x128_f8f6f4 v[152:155], v[26:31], v[20:25], v[152:155], v187, v187 op_sel_hi:[0,0,0] cbsz:2 blgp:2
	v_mfma_scale_f32_16x16x128_f8f6f4 v[148:151], v[2:7], v[32:37], v[148:151], v187, v187 op_sel_hi:[0,0,0] cbsz:2 blgp:2
	v_mfma_scale_f32_16x16x128_f8f6f4 v[140:143], v[8:13], v[32:37], v[140:143], v187, v187 op_sel_hi:[0,0,0] cbsz:2 blgp:2
	v_mfma_scale_f32_16x16x128_f8f6f4 v[132:135], v[14:19], v[32:37], v[132:135], v187, v187 op_sel_hi:[0,0,0] cbsz:2 blgp:2
	v_mfma_scale_f32_16x16x128_f8f6f4 v[124:127], v[26:31], v[32:37], v[124:127], v187, v187 op_sel_hi:[0,0,0] cbsz:2 blgp:2
	s_cmp_eq_u32 s66, 0
	s_cbranch_scc0 .Lst2_other
	s_mov_b64 s[38:39], s[2:3]
	s_mov_b32 s40, s11
	s_mov_b32 s41, s35
	s_waitcnt vmcnt(0)
	s_barrier
	s_mov_b32 m0, s60
	s_nop 0
	global_load_lds_dwordx4 v228, s[38:39]
	s_mov_b32 m0, s61
	s_nop 0
	global_load_lds_dwordx4 v229, s[38:39]
	s_mov_b32 m0, s62
	s_nop 0
	global_load_lds_dwordx4 v230, s[38:39]
	s_mov_b32 m0, s63
	s_nop 0
	global_load_lds_dwordx4 v228, s[40:41]
	s_mov_b32 m0, s64
	s_nop 0
	global_load_lds_dwordx4 v229, s[40:41]
	s_mov_b32 m0, s65
	s_nop 0
	global_load_lds_dwordx4 v230, s[40:41]
	s_branch .Lst2_join

.Lst3_join:
	v_mfma_scale_f32_16x16x128_f8f6f4 v[80:83], v[46:51], v[40:45], v[80:83], v187, v187 op_sel_hi:[0,0,0] cbsz:2 blgp:2
	v_mfma_scale_f32_16x16x128_f8f6f4 v[72:75], v[194:199], v[40:45], v[72:75], v187, v187 op_sel_hi:[0,0,0] cbsz:2 blgp:2
	v_mfma_scale_f32_16x16x128_f8f6f4 v[64:67], v[200:205], v[40:45], v[64:67], v187, v187 op_sel_hi:[0,0,0] cbsz:2 blgp:2
	v_mfma_scale_f32_16x16x128_f8f6f4 v[56:59], v[206:211], v[40:45], v[56:59], v187, v187 op_sel_hi:[0,0,0] cbsz:2 blgp:2
	v_mfma_scale_f32_16x16x128_f8f6f4 v[52:55], v[46:51], v[188:193], v[52:55], v187, v187 op_sel_hi:[0,0,0] cbsz:2 blgp:2
	v_mfma_scale_f32_16x16x128_f8f6f4 v[48:51], v[194:199], v[188:193], v[224:227], v187, v187 op_sel_hi:[0,0,0] cbsz:2 blgp:2
	v_mfma_scale_f32_16x16x128_f8f6f4 v[44:47], v[200:205], v[188:193], v[212:215], v187, v187 op_sel_hi:[0,0,0] cbsz:2 blgp:2
	v_mfma_scale_f32_16x16x128_f8f6f4 v[40:43], v[206:211], v[188:193], v[216:219], v187, v187 op_sel_hi:[0,0,0] cbsz:2 blgp:2
	s_add_i32 s36, s36, 2
	s_add_u32 s11, s11, 0xc000
	s_addc_u32 s35, s35, 0
	s_add_u32 s2, s2, 0xc000
	s_addc_u32 s3, s3, 0
	s_cmp_lt_u32 s36, 4
	s_waitcnt lgkmcnt(0)
	s_cbranch_scc1 .LBB1_3
	s_mov_b32 s2, 1
	s_cmp_lt_i32 s2, 1
	s_cbranch_scc1 .LBB1_6
.LBB1_5:
	ds_read_b128 v[188:191], v1 offset:24576
	ds_read_b64 v[192:193], v172 offset:24640
	ds_read_b128 v[194:197], v1 offset:26112
	ds_read_b64 v[198:199], v172 offset:26176
	ds_read_b128 v[200:203], v170 offset:36864
	ds_read_b64 v[204:205], v173 offset:36928
	ds_read_b128 v[206:209], v170 offset:38400
	ds_read_b64 v[210:211], v173 offset:38464
	ds_read_b128 v[212:215], v170 offset:39936
	ds_read_b64 v[216:217], v173 offset:40000
	ds_read_b128 v[218:221], v170 offset:41472
	ds_read_b64 v[222:223], v173 offset:41536
	v_mfma_scale_f32_16x16x128_f8f6f4 v[164:167], v[2:7], v[20:25], v[164:167], v187, v187 op_sel_hi:[0,0,0] cbsz:2 blgp:2
	v_mfma_scale_f32_16x16x128_f8f6f4 v[160:163], v[8:13], v[20:25], v[160:163], v187, v187 op_sel_hi:[0,0,0] cbsz:2 blgp:2
	v_mfma_scale_f32_16x16x128_f8f6f4 v[156:159], v[14:19], v[20:25], v[156:159], v187, v187 op_sel_hi:[0,0,0] cbsz:2 blgp:2
	v_mfma_scale_f32_16x16x128_f8f6f4 v[152:155], v[26:31], v[20:25], v[152:155], v187, v187 op_sel_hi:[0,0,0] cbsz:2 blgp:2
	v_mfma_scale_f32_16x16x128_f8f6f4 v[148:151], v[2:7], v[32:37], v[148:151], v187, v187 op_sel_hi:[0,0,0] cbsz:2 blgp:2
	v_mfma_scale_f32_16x16x128_f8f6f4 v[140:143], v[8:13], v[32:37], v[140:143], v187, v187 op_sel_hi:[0,0,0] cbsz:2 blgp:2
	v_mfma_scale_f32_16x16x128_f8f6f4 v[132:135], v[14:19], v[32:37], v[132:135], v187, v187 op_sel_hi:[0,0,0] cbsz:2 blgp:2
	v_mfma_scale_f32_16x16x128_f8f6f4 v[124:127], v[26:31], v[32:37], v[124:127], v187, v187 op_sel_hi:[0,0,0] cbsz:2 blgp:2
	s_cmp_eq_u32 s66, 0
	s_cbranch_scc0 .Ltail_nowait
	s_waitcnt vmcnt(0)
.Ltail_nowait:
	s_barrier
	s_waitcnt lgkmcnt(0)
	v_mfma_scale_f32_16x16x128_f8f6f4 v[112:115], v[2:7], v[188:193], v[112:115], v187, v187 op_sel_hi:[0,0,0] cbsz:2 blgp:2
	v_mfma_scale_f32_16x16x128_f8f6f4 v[100:103], v[8:13], v[188:193], v[100:103], v187, v187 op_sel_hi:[0,0,0] cbsz:2 blgp:2
	v_mfma_scale_f32_16x16x128_f8f6f4 v[92:95], v[14:19], v[188:193], v[92:95], v187, v187 op_sel_hi:[0,0,0] cbsz:2 blgp:2
	v_mfma_scale_f32_16x16x128_f8f6f4 v[88:91], v[26:31], v[188:193], v[88:91], v187, v187 op_sel_hi:[0,0,0] cbsz:2 blgp:2
	v_mfma_scale_f32_16x16x128_f8f6f4 v[84:87], v[2:7], v[194:199], v[84:87], v187, v187 op_sel_hi:[0,0,0] cbsz:2 blgp:2
	v_mfma_scale_f32_16x16x128_f8f6f4 v[76:79], v[8:13], v[194:199], v[76:79], v187, v187 op_sel_hi:[0,0,0] cbsz:2 blgp:2
	v_mfma_scale_f32_16x16x128_f8f6f4 v[68:71], v[14:19], v[194:199], v[68:71], v187, v187 op_sel_hi:[0,0,0] cbsz:2 blgp:2
	v_mfma_scale_f32_16x16x128_f8f6f4 v[60:63], v[26:31], v[194:199], v[60:63], v187, v187 op_sel_hi:[0,0,0] cbsz:2 blgp:2
	ds_read_b128 v[2:5], v170 offset:61440
	ds_read_b64 v[6:7], v173 offset:61504
	ds_read_b128 v[8:11], v170 offset:62976
	ds_read_b64 v[12:13], v173 offset:63040
	ds_read_b128 v[14:17], v170 offset:64512
	ds_read_b64 v[18:19], v173 offset:64576
	ds_read_b128 v[26:29], v171 offset:53760
	ds_read_b64 v[30:31], v174 offset:53760
	v_mfma_scale_f32_16x16x128_f8f6f4 v[144:147], v[200:205], v[20:25], v[144:147], v187, v187 op_sel_hi:[0,0,0] cbsz:2 blgp:2
	v_mfma_scale_f32_16x16x128_f8f6f4 v[136:139], v[206:211], v[20:25], v[136:139], v187, v187 op_sel_hi:[0,0,0] cbsz:2 blgp:2
	v_mfma_scale_f32_16x16x128_f8f6f4 v[128:131], v[212:217], v[20:25], v[128:131], v187, v187 op_sel_hi:[0,0,0] cbsz:2 blgp:2
	v_mfma_scale_f32_16x16x128_f8f6f4 v[120:123], v[218:223], v[20:25], v[120:123], v187, v187 op_sel_hi:[0,0,0] cbsz:2 blgp:2
	v_mfma_scale_f32_16x16x128_f8f6f4 v[116:119], v[200:205], v[32:37], v[116:119], v187, v187 op_sel_hi:[0,0,0] cbsz:2 blgp:2
	v_mfma_scale_f32_16x16x128_f8f6f4 v[108:111], v[206:211], v[32:37], v[108:111], v187, v187 op_sel_hi:[0,0,0] cbsz:2 blgp:2
	v_mfma_scale_f32_16x16x128_f8f6f4 v[104:107], v[212:217], v[32:37], v[104:107], v187, v187 op_sel_hi:[0,0,0] cbsz:2 blgp:2
	v_mfma_scale_f32_16x16x128_f8f6f4 v[96:99], v[218:223], v[32:37], v[96:99], v187, v187 op_sel_hi:[0,0,0] cbsz:2 blgp:2
	ds_read_b128 v[20:23], v1 offset:49152
	ds_read_b64 v[24:25], v172 offset:49216
	ds_read_b128 v[32:35], v1 offset:50688
	ds_read_b64 v[36:37], v172 offset:50752
	s_waitcnt vmcnt(0)
	s_barrier
	v_mfma_scale_f32_16x16x128_f8f6f4 v[80:83], v[200:205], v[188:193], v[80:83], v187, v187 op_sel_hi:[0,0,0] cbsz:2 blgp:2
	v_mfma_scale_f32_16x16x128_f8f6f4 v[72:75], v[206:211], v[188:193], v[72:75], v187, v187 op_sel_hi:[0,0,0] cbsz:2 blgp:2
	v_mfma_scale_f32_16x16x128_f8f6f4 v[64:67], v[212:217], v[188:193], v[64:67], v187, v187 op_sel_hi:[0,0,0] cbsz:2 blgp:2
	v_mfma_scale_f32_16x16x128_f8f6f4 v[56:59], v[218:223], v[188:193], v[56:59], v187, v187 op_sel_hi:[0,0,0] cbsz:2 blgp:2
	v_mfma_scale_f32_16x16x128_f8f6f4 v[52:55], v[200:205], v[194:199], v[52:55], v187, v187 op_sel_hi:[0,0,0] cbsz:2 blgp:2
	v_mfma_scale_f32_16x16x128_f8f6f4 v[224:227], v[206:211], v[194:199], v[48:51], v187, v187 op_sel_hi:[0,0,0] cbsz:2 blgp:2
	v_mfma_scale_f32_16x16x128_f8f6f4 v[212:215], v[212:217], v[194:199], v[44:47], v187, v187 op_sel_hi:[0,0,0] cbsz:2 blgp:2
	v_mfma_scale_f32_16x16x128_f8f6f4 v[216:219], v[218:223], v[194:199], v[40:43], v187, v187 op_sel_hi:[0,0,0] cbsz:2 blgp:2
	s_waitcnt lgkmcnt(0)
	s_nop 0
	ds_read_b128 v[40:43], v175
	ds_read_b64 v[44:45], v176
	ds_read_b128 v[188:191], v179
	ds_read_b64 v[192:193], v180
	ds_read_b128 v[46:49], v177
	ds_read_b64 v[50:51], v178
	ds_read_b128 v[194:197], v181
	ds_read_b64 v[198:199], v182
	ds_read_b128 v[200:203], v183
	ds_read_b64 v[204:205], v184
	ds_read_b128 v[206:209], v185
	ds_read_b64 v[210:211], v186
	v_mfma_scale_f32_16x16x128_f8f6f4 v[164:167], v[2:7], v[20:25], v[164:167], v187, v187 op_sel_hi:[0,0,0] cbsz:2 blgp:2
	v_mfma_scale_f32_16x16x128_f8f6f4 v[160:163], v[8:13], v[20:25], v[160:163], v187, v187 op_sel_hi:[0,0,0] cbsz:2 blgp:2
	v_mfma_scale_f32_16x16x128_f8f6f4 v[156:159], v[14:19], v[20:25], v[156:159], v187, v187 op_sel_hi:[0,0,0] cbsz:2 blgp:2
	v_mfma_scale_f32_16x16x128_f8f6f4 v[152:155], v[26:31], v[20:25], v[152:155], v187, v187 op_sel_hi:[0,0,0] cbsz:2 blgp:2
	v_mfma_scale_f32_16x16x128_f8f6f4 v[148:151], v[2:7], v[32:37], v[148:151], v187, v187 op_sel_hi:[0,0,0] cbsz:2 blgp:2
	v_mfma_scale_f32_16x16x128_f8f6f4 v[140:143], v[8:13], v[32:37], v[140:143], v187, v187 op_sel_hi:[0,0,0] cbsz:2 blgp:2
	v_mfma_scale_f32_16x16x128_f8f6f4 v[132:135], v[14:19], v[32:37], v[132:135], v187, v187 op_sel_hi:[0,0,0] cbsz:2 blgp:2
	v_mfma_scale_f32_16x16x128_f8f6f4 v[124:127], v[26:31], v[32:37], v[124:127], v187, v187 op_sel_hi:[0,0,0] cbsz:2 blgp:2
	s_waitcnt lgkmcnt(0)
	v_mfma_scale_f32_16x16x128_f8f6f4 v[112:115], v[2:7], v[40:45], v[112:115], v187, v187 op_sel_hi:[0,0,0] cbsz:2 blgp:2
	v_mfma_scale_f32_16x16x128_f8f6f4 v[100:103], v[8:13], v[40:45], v[100:103], v187, v187 op_sel_hi:[0,0,0] cbsz:2 blgp:2
	v_mfma_scale_f32_16x16x128_f8f6f4 v[92:95], v[14:19], v[40:45], v[92:95], v187, v187 op_sel_hi:[0,0,0] cbsz:2 blgp:2
	v_mfma_scale_f32_16x16x128_f8f6f4 v[88:91], v[26:31], v[40:45], v[88:91], v187, v187 op_sel_hi:[0,0,0] cbsz:2 blgp:2
	v_mfma_scale_f32_16x16x128_f8f6f4 v[84:87], v[2:7], v[188:193], v[84:87], v187, v187 op_sel_hi:[0,0,0] cbsz:2 blgp:2
	v_mfma_scale_f32_16x16x128_f8f6f4 v[76:79], v[8:13], v[188:193], v[76:79], v187, v187 op_sel_hi:[0,0,0] cbsz:2 blgp:2
	v_mfma_scale_f32_16x16x128_f8f6f4 v[68:71], v[14:19], v[188:193], v[68:71], v187, v187 op_sel_hi:[0,0,0] cbsz:2 blgp:2
	v_mfma_scale_f32_16x16x128_f8f6f4 v[60:63], v[26:31], v[188:193], v[60:63], v187, v187 op_sel_hi:[0,0,0] cbsz:2 blgp:2
	v_mfma_scale_f32_16x16x128_f8f6f4 v[144:147], v[46:51], v[20:25], v[144:147], v187, v187 op_sel_hi:[0,0,0] cbsz:2 blgp:2
	v_mfma_scale_f32_16x16x128_f8f6f4 v[136:139], v[194:199], v[20:25], v[136:139], v187, v187 op_sel_hi:[0,0,0] cbsz:2 blgp:2
	v_mfma_scale_f32_16x16x128_f8f6f4 v[128:131], v[200:205], v[20:25], v[128:131], v187, v187 op_sel_hi:[0,0,0] cbsz:2 blgp:2
	v_mfma_scale_f32_16x16x128_f8f6f4 v[120:123], v[206:211], v[20:25], v[120:123], v187, v187 op_sel_hi:[0,0,0] cbsz:2 blgp:2
	v_mfma_scale_f32_16x16x128_f8f6f4 v[116:119], v[46:51], v[32:37], v[116:119], v187, v187 op_sel_hi:[0,0,0] cbsz:2 blgp:2
	v_mfma_scale_f32_16x16x128_f8f6f4 v[108:111], v[194:199], v[32:37], v[108:111], v187, v187 op_sel_hi:[0,0,0] cbsz:2 blgp:2
	v_mfma_scale_f32_16x16x128_f8f6f4 v[104:107], v[200:205], v[32:37], v[104:107], v187, v187 op_sel_hi:[0,0,0] cbsz:2 blgp:2
	v_mfma_scale_f32_16x16x128_f8f6f4 v[96:99], v[206:211], v[32:37], v[96:99], v187, v187 op_sel_hi:[0,0,0] cbsz:2 blgp:2
	v_mfma_scale_f32_16x16x128_f8f6f4 v[80:83], v[46:51], v[40:45], v[80:83], v187, v187 op_sel_hi:[0,0,0] cbsz:2 blgp:2
	v_mfma_scale_f32_16x16x128_f8f6f4 v[72:75], v[194:199], v[40:45], v[72:75], v187, v187 op_sel_hi:[0,0,0] cbsz:2 blgp:2
	v_mfma_scale_f32_16x16x128_f8f6f4 v[64:67], v[200:205], v[40:45], v[64:67], v187, v187 op_sel_hi:[0,0,0] cbsz:2 blgp:2
	v_mfma_scale_f32_16x16x128_f8f6f4 v[56:59], v[206:211], v[40:45], v[56:59], v187, v187 op_sel_hi:[0,0,0] cbsz:2 blgp:2
	v_mfma_scale_f32_16x16x128_f8f6f4 v[52:55], v[46:51], v[188:193], v[52:55], v187, v187 op_sel_hi:[0,0,0] cbsz:2 blgp:2
	v_mfma_scale_f32_16x16x128_f8f6f4 v[48:51], v[194:199], v[188:193], v[224:227], v187, v187 op_sel_hi:[0,0,0] cbsz:2 blgp:2
	v_mfma_scale_f32_16x16x128_f8f6f4 v[44:47], v[200:205], v[188:193], v[212:215], v187, v187 op_sel_hi:[0,0,0] cbsz:2 blgp:2
	v_mfma_scale_f32_16x16x128_f8f6f4 v[40:43], v[206:211], v[188:193], v[216:219], v187, v187 op_sel_hi:[0,0,0] cbsz:2 blgp:2
	s_add_i32 s2, s2, -1
	s_cmp_lg_u32 s2, 0
	s_cbranch_scc1 .LBB1_5
